# baseline (speedup 1.0000x reference)
.Lk1_nowarm0:
	s_waitcnt lgkmcnt(0)
	s_add_u32 s8, s4, s17
	s_addc_u32 s9, s5, s20
	s_and_b32 s9, s9, 0xffff
	s_cmp_eq_u32 s21, 9
	s_cselect_b32 s17, 1, 0
	s_cmp_eq_u32 s16, 0
	s_cselect_b32 s17, s17, 0
	s_cmp_lg_u32 s17, 0
	s_cbranch_scc0 .Lk1_nowarm9
	s_mul_i32 s22, s15, 0x3a9800
	v_writelane_b32 v3, s22, 0
	s_add_u32 s23, s22, 0x10000
	v_writelane_b32 v3, s23, 1
	s_add_u32 s22, s22, 0x138800
	v_writelane_b32 v3, s22, 2
	s_add_u32 s23, s22, 0x10000
	v_writelane_b32 v3, s23, 3
	s_add_u32 s22, s22, 0x138800
	v_writelane_b32 v3, s22, 4
	s_add_u32 s23, s22, 0x10000
	v_writelane_b32 v3, s23, 5
	s_mov_b64 exec, 63
	global_load_dword v92, v3, s[32:33]
	s_mul_i32 s22, s15, 0x12c00
	s_add_u32 s22, s22, 0x1c200
	v_writelane_b32 v3, s22, 0
	s_add_u32 s22, s22, 0x10000
	v_writelane_b32 v3, s22, 1
	s_mul_i32 s22, s15, 0xe10
	v_writelane_b32 v3, s22, 2
	s_mul_i32 s22, s15, 0x4b0
	s_add_u32 s22, s22, 0x274200
	v_writelane_b32 v3, s22, 3
	s_mov_b64 exec, 15
	global_load_dword v93, v3, s[34:35]
	s_mov_b64 exec, s[18:19]
.Lk1_nowarm9:
	s_mov_b32 s40, 0
	s_add_u32 s41, s40, s13
	s_add_u32 s42, s41, s13
	s_add_u32 s43, s42, s13
	s_add_u32 s44, s43, s13
	s_add_u32 s45, s44, s13
	s_add_u32 s46, s45, s13
	s_add_u32 s47, s46, s13
	s_add_u32 s48, s47, s13
	s_add_u32 s49, s48, s13
	s_add_u32 s50, s49, s13
	s_add_u32 s51, s50, s13
	s_add_u32 s52, s51, s13
	s_add_u32 s53, s52, s13
	s_add_u32 s54, s53, s13
	s_add_u32 s55, s54, s13
	buffer_load_dword v8, v1, s[8:11], s40 offen nt
	buffer_load_dword v9, v1, s[8:11], s41 offen nt
	buffer_load_dword v10, v1, s[8:11], s42 offen nt
	buffer_load_dword v11, v1, s[8:11], s43 offen nt
	buffer_load_dword v12, v1, s[8:11], s44 offen nt
	buffer_load_dword v13, v1, s[8:11], s45 offen nt
	buffer_load_dword v14, v1, s[8:11], s46 offen nt
	buffer_load_dword v15, v1, s[8:11], s47 offen nt
	buffer_load_dword v16, v1, s[8:11], s48 offen nt
	buffer_load_dword v17, v1, s[8:11], s49 offen nt
	buffer_load_dword v18, v1, s[8:11], s50 offen nt
	buffer_load_dword v19, v1, s[8:11], s51 offen nt
	buffer_load_dword v20, v1, s[8:11], s52 offen nt
	buffer_load_dword v21, v1, s[8:11], s53 offen nt
	buffer_load_dword v22, v1, s[8:11], s54 offen nt
	buffer_load_dword v23, v1, s[8:11], s55 offen nt
	s_add_u32 s8, s8, 0x4e200
	s_addc_u32 s9, s9, 0
	buffer_load_dword v24, v1, s[8:11], s40 offen nt
	buffer_load_dword v25, v1, s[8:11], s41 offen nt
	buffer_load_dword v26, v1, s[8:11], s42 offen nt
	buffer_load_dword v27, v1, s[8:11], s43 offen nt
	buffer_load_dword v28, v1, s[8:11], s44 offen nt
	buffer_load_dword v29, v1, s[8:11], s45 offen nt
	buffer_load_dword v30, v1, s[8:11], s46 offen nt
	buffer_load_dword v31, v1, s[8:11], s47 offen nt
	buffer_load_dword v32, v1, s[8:11], s48 offen nt
	buffer_load_dword v33, v1, s[8:11], s49 offen nt
	buffer_load_dword v34, v1, s[8:11], s50 offen nt
	buffer_load_dword v35, v1, s[8:11], s51 offen nt
	buffer_load_dword v36, v1, s[8:11], s52 offen nt
	buffer_load_dword v37, v1, s[8:11], s53 offen nt
	buffer_load_dword v38, v1, s[8:11], s54 offen nt
	buffer_load_dword v39, v1, s[8:11], s55 offen nt
	s_add_u32 s8, s8, 0x4e200
	s_addc_u32 s9, s9, 0
	buffer_load_dword v40, v1, s[8:11], s40 offen nt
	buffer_load_dword v41, v1, s[8:11], s41 offen nt
	buffer_load_dword v42, v1, s[8:11], s42 offen nt
	buffer_load_dword v43, v1, s[8:11], s43 offen nt
	buffer_load_dword v44, v1, s[8:11], s44 offen nt
	buffer_load_dword v45, v1, s[8:11], s45 offen nt
	buffer_load_dword v46, v1, s[8:11], s46 offen nt
	buffer_load_dword v47, v1, s[8:11], s47 offen nt
	buffer_load_dword v48, v1, s[8:11], s48 offen nt
	buffer_load_dword v49, v1, s[8:11], s49 offen nt
	buffer_load_dword v50, v1, s[8:11], s50 offen nt
	buffer_load_dword v51, v1, s[8:11], s51 offen nt
	buffer_load_dword v52, v1, s[8:11], s52 offen nt
	buffer_load_dword v53, v1, s[8:11], s53 offen nt
	buffer_load_dword v54, v1, s[8:11], s54 offen nt
	buffer_load_dword v55, v1, s[8:11], s55 offen nt
	v_mul_u32_u24_e32 v3, 0x147b, v2
	v_lshrrev_b32_e32 v3, 19, v3
	v_mul_u32_u24_e32 v98, 0x64, v3
	v_sub_u32_e32 v98, v2, v98
	v_add_u32_e32 v3, -1, v3
	v_add_u32_e32 v98, -1, v98
	s_movk_i32 s17, 0x62
	v_cmp_gt_u32_e64 s[36:37], 48, v3
	v_cmp_gt_u32_e64 s[38:39], s17, v98
	s_mul_i32 s17, s15, 0x1388
	v_add_lshl_u32 v98, v2, s17, 3
	s_and_b64 s[36:37], s[36:37], s[38:39]
	s_waitcnt vmcnt(32)
	v_max3_f32 v76, v8, v9, v10
	v_max3_f32 v76, v76, v11, v12
	v_max3_f32 v76, v76, v13, v14
	v_max3_f32 v76, v76, v15, v16
	v_max3_f32 v76, v76, v17, v18
	v_max3_f32 v76, v76, v19, v20
	v_max3_f32 v76, v76, v21, v22
	v_max_f32_e32 v76, v76, v23
	v_sub_f32_e32 v8, v8, v76
	v_sub_f32_e32 v9, v9, v76
	v_sub_f32_e32 v10, v10, v76
	v_sub_f32_e32 v11, v11, v76
	v_sub_f32_e32 v12, v12, v76
	v_sub_f32_e32 v13, v13, v76
	v_sub_f32_e32 v14, v14, v76
	v_sub_f32_e32 v15, v15, v76
	v_sub_f32_e32 v16, v16, v76
	v_sub_f32_e32 v17, v17, v76
	v_sub_f32_e32 v18, v18, v76
	v_sub_f32_e32 v19, v19, v76
	v_sub_f32_e32 v20, v20, v76
	v_sub_f32_e32 v21, v21, v76
	v_sub_f32_e32 v22, v22, v76
	v_sub_f32_e32 v23, v23, v76
	v_or_b32_e32 v81, 0, v8
	v_or_b32_e32 v82, 1, v9
	v_min_u32_e32 v80, v81, v82
	v_or_b32_e32 v81, 2, v10
	v_or_b32_e32 v82, 3, v11
	v_min3_u32 v80, v80, v81, v82
	v_or_b32_e32 v81, 4, v12
	v_or_b32_e32 v82, 5, v13
	v_min3_u32 v80, v80, v81, v82
	v_or_b32_e32 v81, 6, v14
	v_or_b32_e32 v82, 7, v15
	v_min3_u32 v80, v80, v81, v82
	v_or_b32_e32 v81, 8, v16
	v_or_b32_e32 v82, 9, v17
	v_min3_u32 v80, v80, v81, v82
	v_or_b32_e32 v81, 10, v18
	v_or_b32_e32 v82, 11, v19
	v_min3_u32 v80, v80, v81, v82
	v_or_b32_e32 v81, 12, v20
	v_or_b32_e32 v82, 13, v21
	v_min3_u32 v80, v80, v81, v82
	v_or_b32_e32 v81, 14, v22
	v_or_b32_e32 v82, 15, v23
	v_min3_u32 v80, v80, v81, v82
	v_mul_f32_e32 v8, s14, v8
	v_mul_f32_e32 v9, s14, v9
	v_mul_f32_e32 v10, s14, v10
	v_mul_f32_e32 v11, s14, v11
	v_mul_f32_e32 v12, s14, v12
	v_mul_f32_e32 v13, s14, v13
	v_mul_f32_e32 v14, s14, v14
	v_mul_f32_e32 v15, s14, v15
	v_mul_f32_e32 v16, s14, v16
	v_mul_f32_e32 v17, s14, v17
	v_mul_f32_e32 v18, s14, v18
	v_mul_f32_e32 v19, s14, v19
	v_mul_f32_e32 v20, s14, v20
	v_mul_f32_e32 v21, s14, v21
	v_mul_f32_e32 v22, s14, v22
	v_mul_f32_e32 v23, s14, v23
	v_exp_f32_e32 v8, v8
	v_exp_f32_e32 v9, v9
	v_exp_f32_e32 v10, v10
	v_exp_f32_e32 v11, v11
	v_exp_f32_e32 v12, v12
	v_exp_f32_e32 v13, v13
	v_exp_f32_e32 v14, v14
	v_exp_f32_e32 v15, v15
	v_exp_f32_e32 v16, v16
	v_exp_f32_e32 v17, v17
	v_exp_f32_e32 v18, v18
	v_exp_f32_e32 v19, v19
	v_exp_f32_e32 v20, v20
	v_exp_f32_e32 v21, v21
	v_exp_f32_e32 v22, v22
	v_exp_f32_e32 v23, v23
	v_add_f32_e32 v78, v8, v10
	v_add_f32_e32 v79, v9, v11
	v_add_f32_e32 v78, v78, v12
	v_add_f32_e32 v79, v79, v13
	v_add_f32_e32 v78, v78, v14
	v_add_f32_e32 v79, v79, v15
	v_add_f32_e32 v78, v78, v16
	v_add_f32_e32 v79, v79, v17
	v_add_f32_e32 v78, v78, v18
	v_add_f32_e32 v79, v79, v19
	v_add_f32_e32 v78, v78, v20
	v_add_f32_e32 v79, v79, v21
	v_add_f32_e32 v78, v78, v22
	v_add_f32_e32 v79, v79, v23
	v_add_f32_e32 v78, v78, v79
	v_cvt_f64_f32_e32 v[86:87], v78
	v_mov_b32_e32 v75, v80
	v_mov_b32_e32 v73, v76
	s_add_u32 s8, s8, 0x4e200
	s_addc_u32 s9, s9, 0
	buffer_load_dword v56, v1, s[8:11], s40 offen nt
	buffer_load_dword v57, v1, s[8:11], s41 offen nt
	buffer_load_dword v58, v1, s[8:11], s42 offen nt
	buffer_load_dword v59, v1, s[8:11], s43 offen nt
	buffer_load_dword v60, v1, s[8:11], s44 offen nt
	buffer_load_dword v61, v1, s[8:11], s45 offen nt
	buffer_load_dword v62, v1, s[8:11], s46 offen nt
	buffer_load_dword v63, v1, s[8:11], s47 offen nt
	buffer_load_dword v64, v1, s[8:11], s48 offen nt
	buffer_load_dword v65, v1, s[8:11], s49 offen nt
	buffer_load_dword v66, v1, s[8:11], s50 offen nt
	buffer_load_dword v67, v1, s[8:11], s51 offen nt
	buffer_load_dword v68, v1, s[8:11], s52 offen nt
	buffer_load_dword v69, v1, s[8:11], s53 offen nt
	buffer_load_dword v70, v1, s[8:11], s54 offen nt
	buffer_load_dword v71, v1, s[8:11], s55 offen nt
	s_add_u32 s8, s8, 0x4e200
	s_addc_u32 s9, s9, 0
	buffer_load_dword v72, v1, s[8:11], s40 offen nt
	s_waitcnt vmcnt(33)
	v_max3_f32 v76, v24, v25, v26
	v_max3_f32 v76, v76, v27, v28
	v_max3_f32 v76, v76, v29, v30
	v_max3_f32 v76, v76, v31, v32
	v_max3_f32 v76, v76, v33, v34
	v_max3_f32 v76, v76, v35, v36
	v_max3_f32 v76, v76, v37, v38
	v_max_f32_e32 v76, v76, v39
	v_max_f32_e32 v77, v73, v76
	v_cmp_gt_f32_e64 s[20:21], v76, v73
	v_sub_f32_e32 v83, v73, v77
	v_mul_f32_e32 v83, s14, v83
	v_exp_f32_e32 v83, v83
	v_sub_f32_e32 v24, v24, v77
	v_sub_f32_e32 v25, v25, v77
	v_sub_f32_e32 v26, v26, v77
	v_sub_f32_e32 v27, v27, v77
	v_sub_f32_e32 v28, v28, v77
	v_sub_f32_e32 v29, v29, v77
	v_sub_f32_e32 v30, v30, v77
	v_sub_f32_e32 v31, v31, v77
	v_sub_f32_e32 v32, v32, v77
	v_sub_f32_e32 v33, v33, v77
	v_sub_f32_e32 v34, v34, v77
	v_sub_f32_e32 v35, v35, v77
	v_sub_f32_e32 v36, v36, v77
	v_sub_f32_e32 v37, v37, v77
	v_sub_f32_e32 v38, v38, v77
	v_sub_f32_e32 v39, v39, v77
	v_cvt_f64_f32_e32 v[84:85], v83
	v_or_b32_e32 v81, 16, v24
	v_or_b32_e32 v82, 17, v25
	v_min_u32_e32 v80, v81, v82
	v_or_b32_e32 v81, 18, v26
	v_or_b32_e32 v82, 19, v27
	v_min3_u32 v80, v80, v81, v82
	v_or_b32_e32 v81, 20, v28
	v_or_b32_e32 v82, 21, v29
	v_min3_u32 v80, v80, v81, v82
	v_or_b32_e32 v81, 22, v30
	v_or_b32_e32 v82, 23, v31
	v_min3_u32 v80, v80, v81, v82
	v_or_b32_e32 v81, 24, v32
	v_or_b32_e32 v82, 25, v33
	v_min3_u32 v80, v80, v81, v82
	v_or_b32_e32 v81, 26, v34
	v_or_b32_e32 v82, 27, v35
	v_min3_u32 v80, v80, v81, v82
	v_or_b32_e32 v81, 28, v36
	v_or_b32_e32 v82, 29, v37
	v_min3_u32 v80, v80, v81, v82
	v_or_b32_e32 v81, 30, v38
	v_or_b32_e32 v82, 31, v39
	v_min3_u32 v80, v80, v81, v82
	v_mul_f64 v[86:87], v[86:87], v[84:85]
	v_mul_f32_e32 v24, s14, v24
	v_mul_f32_e32 v25, s14, v25
	v_mul_f32_e32 v26, s14, v26
	v_mul_f32_e32 v27, s14, v27
	v_mul_f32_e32 v28, s14, v28
	v_mul_f32_e32 v29, s14, v29
	v_mul_f32_e32 v30, s14, v30
	v_mul_f32_e32 v31, s14, v31
	v_mul_f32_e32 v32, s14, v32
	v_mul_f32_e32 v33, s14, v33
	v_mul_f32_e32 v34, s14, v34
	v_mul_f32_e32 v35, s14, v35
	v_mul_f32_e32 v36, s14, v36
	v_mul_f32_e32 v37, s14, v37
	v_mul_f32_e32 v38, s14, v38
	v_mul_f32_e32 v39, s14, v39
	v_exp_f32_e32 v24, v24
	v_exp_f32_e32 v25, v25
	v_exp_f32_e32 v26, v26
	v_exp_f32_e32 v27, v27
	v_exp_f32_e32 v28, v28
	v_exp_f32_e32 v29, v29
	v_exp_f32_e32 v30, v30
	v_exp_f32_e32 v31, v31
	v_exp_f32_e32 v32, v32
	v_exp_f32_e32 v33, v33
	v_exp_f32_e32 v34, v34
	v_exp_f32_e32 v35, v35
	v_exp_f32_e32 v36, v36
	v_exp_f32_e32 v37, v37
	v_exp_f32_e32 v38, v38
	v_exp_f32_e32 v39, v39
	v_add_f32_e32 v78, v24, v26
	v_add_f32_e32 v79, v25, v27
	v_add_f32_e32 v78, v78, v28
	v_add_f32_e32 v79, v79, v29
	v_add_f32_e32 v78, v78, v30
	v_add_f32_e32 v79, v79, v31
	v_add_f32_e32 v78, v78, v32
	v_add_f32_e32 v79, v79, v33
	v_add_f32_e32 v78, v78, v34
	v_add_f32_e32 v79, v79, v35
	v_add_f32_e32 v78, v78, v36
	v_add_f32_e32 v79, v79, v37
	v_add_f32_e32 v78, v78, v38
	v_add_f32_e32 v79, v79, v39
	v_add_f32_e32 v78, v78, v79
	v_cvt_f64_f32_e32 v[84:85], v78
	v_cndmask_b32_e64 v75, v75, v80, s[20:21]
	v_mov_b32_e32 v73, v77
	v_add_f64 v[86:87], v[86:87], v[84:85]
	s_waitcnt vmcnt(17)
	v_max3_f32 v76, v40, v41, v42
	v_max3_f32 v76, v76, v43, v44
	v_max3_f32 v76, v76, v45, v46
	v_max3_f32 v76, v76, v47, v48
	v_max3_f32 v76, v76, v49, v50
	v_max3_f32 v76, v76, v51, v52
	v_max3_f32 v76, v76, v53, v54
	v_max_f32_e32 v76, v76, v55
	v_max_f32_e32 v77, v73, v76
	v_cmp_gt_f32_e64 s[20:21], v76, v73
	v_sub_f32_e32 v83, v73, v77
	v_mul_f32_e32 v83, s14, v83
	v_exp_f32_e32 v83, v83
	v_sub_f32_e32 v40, v40, v77
	v_sub_f32_e32 v41, v41, v77
	v_sub_f32_e32 v42, v42, v77
	v_sub_f32_e32 v43, v43, v77
	v_sub_f32_e32 v44, v44, v77
	v_sub_f32_e32 v45, v45, v77
	v_sub_f32_e32 v46, v46, v77
	v_sub_f32_e32 v47, v47, v77
	v_sub_f32_e32 v48, v48, v77
	v_sub_f32_e32 v49, v49, v77
	v_sub_f32_e32 v50, v50, v77
	v_sub_f32_e32 v51, v51, v77
	v_sub_f32_e32 v52, v52, v77
	v_sub_f32_e32 v53, v53, v77
	v_sub_f32_e32 v54, v54, v77
	v_sub_f32_e32 v55, v55, v77
	v_cvt_f64_f32_e32 v[84:85], v83
	v_or_b32_e32 v81, 32, v40
	v_or_b32_e32 v82, 33, v41
	v_min_u32_e32 v80, v81, v82
	v_or_b32_e32 v81, 34, v42
	v_or_b32_e32 v82, 35, v43
	v_min3_u32 v80, v80, v81, v82
	v_or_b32_e32 v81, 36, v44
	v_or_b32_e32 v82, 37, v45
	v_min3_u32 v80, v80, v81, v82
	v_or_b32_e32 v81, 38, v46
	v_or_b32_e32 v82, 39, v47
	v_min3_u32 v80, v80, v81, v82
	v_or_b32_e32 v81, 40, v48
	v_or_b32_e32 v82, 41, v49
	v_min3_u32 v80, v80, v81, v82
	v_or_b32_e32 v81, 42, v50
	v_or_b32_e32 v82, 43, v51
	v_min3_u32 v80, v80, v81, v82
	v_or_b32_e32 v81, 44, v52
	v_or_b32_e32 v82, 45, v53
	v_min3_u32 v80, v80, v81, v82
	v_or_b32_e32 v81, 46, v54
	v_or_b32_e32 v82, 47, v55
	v_min3_u32 v80, v80, v81, v82
	v_mul_f64 v[86:87], v[86:87], v[84:85]
	v_mul_f32_e32 v40, s14, v40
	v_mul_f32_e32 v41, s14, v41
	v_mul_f32_e32 v42, s14, v42
	v_mul_f32_e32 v43, s14, v43
	v_mul_f32_e32 v44, s14, v44
	v_mul_f32_e32 v45, s14, v45
	v_mul_f32_e32 v46, s14, v46
	v_mul_f32_e32 v47, s14, v47
	v_mul_f32_e32 v48, s14, v48
	v_mul_f32_e32 v49, s14, v49
	v_mul_f32_e32 v50, s14, v50
	v_mul_f32_e32 v51, s14, v51
	v_mul_f32_e32 v52, s14, v52
	v_mul_f32_e32 v53, s14, v53
	v_mul_f32_e32 v54, s14, v54
	v_mul_f32_e32 v55, s14, v55
	v_exp_f32_e32 v40, v40
	v_exp_f32_e32 v41, v41
	v_exp_f32_e32 v42, v42
	v_exp_f32_e32 v43, v43
	v_exp_f32_e32 v44, v44
	v_exp_f32_e32 v45, v45
	v_exp_f32_e32 v46, v46
	v_exp_f32_e32 v47, v47
	v_exp_f32_e32 v48, v48
	v_exp_f32_e32 v49, v49
	v_exp_f32_e32 v50, v50
	v_exp_f32_e32 v51, v51
	v_exp_f32_e32 v52, v52
	v_exp_f32_e32 v53, v53
	v_exp_f32_e32 v54, v54
	v_exp_f32_e32 v55, v55
	v_add_f32_e32 v78, v40, v42
	v_add_f32_e32 v79, v41, v43
	v_add_f32_e32 v78, v78, v44
	v_add_f32_e32 v79, v79, v45
	v_add_f32_e32 v78, v78, v46
	v_add_f32_e32 v79, v79, v47
	v_add_f32_e32 v78, v78, v48
	v_add_f32_e32 v79, v79, v49
	v_add_f32_e32 v78, v78, v50
	v_add_f32_e32 v79, v79, v51
	v_add_f32_e32 v78, v78, v52
	v_add_f32_e32 v79, v79, v53
	v_add_f32_e32 v78, v78, v54
	v_add_f32_e32 v79, v79, v55
	v_add_f32_e32 v78, v78, v79
	v_cvt_f64_f32_e32 v[84:85], v78
	v_cndmask_b32_e64 v75, v75, v80, s[20:21]
	v_mov_b32_e32 v73, v77
	v_add_f64 v[86:87], v[86:87], v[84:85]
	s_cmp_eq_u32 s21, 2
	s_cselect_b32 s17, 1, 0
	s_cmp_eq_u32 s16, 4
	s_cselect_b32 s17, s17, 0
	s_cmp_lg_u32 s17, 0
	s_cbranch_scc0 .Lk1_nopiv
	v_cvt_f32_f64_e32 v3, v[86:87]
	s_mov_b32 s22, 0
	v_rcp_f32_e32 v3, v3
	s_mov_b32 s23, 0x20000000
	v_mul_f32_e32 v3, 0x3f3d0bd1, v3
.Lk1_piv:
	s_or_b32 s24, s22, s23
	v_cmp_le_u32_e32 vcc, s24, v3
	s_lshr_b32 s23, s23, 1
	s_bcnt1_i32_b64 s25, vcc
	s_cmp_ge_u32 s25, 16
	s_cselect_b32 s22, s24, s22
	s_cmp_ge_u32 s23, 0x4000
	s_cbranch_scc1 .Lk1_piv
	s_lshl_b32 s23, s15, 2
	s_add_u32 s23, s23, 0x138800
	v_mov_b32_e32 v3, s23
	v_mov_b32_e32 v81, s22
	s_mov_b64 exec, 1
	global_store_dword v3, v81, s[6:7]
	s_mov_b64 exec, s[18:19]
.Lk1_nopiv:
	s_waitcnt vmcnt(5)
	v_max3_f32 v76, v56, v57, v58
	v_max3_f32 v76, v76, v59, v60
	v_max3_f32 v76, v76, v61, v62
	v_max3_f32 v76, v76, v63, v64
	v_max3_f32 v76, v76, v65, v66
	v_max_f32_e32 v76, v76, v67
	v_max_f32_e32 v77, v73, v76
	v_cmp_gt_f32_e64 s[20:21], v76, v73
	v_sub_f32_e32 v83, v73, v77
	v_mul_f32_e32 v83, s14, v83
	v_exp_f32_e32 v83, v83
	v_sub_f32_e32 v56, v56, v77
	v_sub_f32_e32 v57, v57, v77
	v_sub_f32_e32 v58, v58, v77
	v_sub_f32_e32 v59, v59, v77
	v_sub_f32_e32 v60, v60, v77
	v_sub_f32_e32 v61, v61, v77
	v_sub_f32_e32 v62, v62, v77
	v_sub_f32_e32 v63, v63, v77
	v_sub_f32_e32 v64, v64, v77
	v_sub_f32_e32 v65, v65, v77
	v_sub_f32_e32 v66, v66, v77
	v_sub_f32_e32 v67, v67, v77
	v_cvt_f64_f32_e32 v[84:85], v83
	v_or_b32_e32 v81, 48, v56
	v_or_b32_e32 v82, 49, v57
	v_min_u32_e32 v80, v81, v82
	v_or_b32_e32 v81, 50, v58
	v_or_b32_e32 v82, 51, v59
	v_min3_u32 v80, v80, v81, v82
	v_or_b32_e32 v81, 52, v60
	v_or_b32_e32 v82, 53, v61
	v_min3_u32 v80, v80, v81, v82
	v_or_b32_e32 v81, 54, v62
	v_or_b32_e32 v82, 55, v63
	v_min3_u32 v80, v80, v81, v82
	v_or_b32_e32 v81, 56, v64
	v_or_b32_e32 v82, 57, v65
	v_min3_u32 v80, v80, v81, v82
	v_or_b32_e32 v81, 58, v66
	v_or_b32_e32 v82, 59, v67
	v_min3_u32 v80, v80, v81, v82
	v_mul_f64 v[86:87], v[86:87], v[84:85]
	v_mul_f32_e32 v56, s14, v56
	v_mul_f32_e32 v57, s14, v57
	v_mul_f32_e32 v58, s14, v58
	v_mul_f32_e32 v59, s14, v59
	v_mul_f32_e32 v60, s14, v60
	v_mul_f32_e32 v61, s14, v61
	v_mul_f32_e32 v62, s14, v62
	v_mul_f32_e32 v63, s14, v63
	v_mul_f32_e32 v64, s14, v64
	v_mul_f32_e32 v65, s14, v65
	v_mul_f32_e32 v66, s14, v66
	v_mul_f32_e32 v67, s14, v67
	v_exp_f32_e32 v56, v56
	v_exp_f32_e32 v57, v57
	v_exp_f32_e32 v58, v58
	v_exp_f32_e32 v59, v59
	v_exp_f32_e32 v60, v60
	v_exp_f32_e32 v61, v61
	v_exp_f32_e32 v62, v62
	v_exp_f32_e32 v63, v63
	v_exp_f32_e32 v64, v64
	v_exp_f32_e32 v65, v65
	v_exp_f32_e32 v66, v66
	v_exp_f32_e32 v67, v67
	v_add_f32_e32 v78, v56, v58
	v_add_f32_e32 v79, v57, v59
	v_add_f32_e32 v78, v78, v60
	v_add_f32_e32 v79, v79, v61
	v_add_f32_e32 v78, v78, v62
	v_add_f32_e32 v79, v79, v63
	v_add_f32_e32 v78, v78, v64
	v_add_f32_e32 v79, v79, v65
	v_add_f32_e32 v78, v78, v66
	v_add_f32_e32 v79, v79, v67
	v_add_f32_e32 v78, v78, v79
	v_cvt_f64_f32_e32 v[84:85], v78
	v_cndmask_b32_e64 v75, v75, v80, s[20:21]
	v_mov_b32_e32 v73, v77
	v_add_f64 v[86:87], v[86:87], v[84:85]
	s_waitcnt vmcnt(0)
	v_max3_f32 v76, v68, v69, v70
	v_max3_f32 v76, v76, v71, v72
	v_max_f32_e32 v77, v73, v76
	v_cmp_gt_f32_e64 s[20:21], v76, v73
	v_sub_f32_e32 v83, v73, v77
	v_mul_f32_e32 v83, s14, v83
	v_exp_f32_e32 v83, v83
	v_sub_f32_e32 v68, v68, v77
	v_sub_f32_e32 v69, v69, v77
	v_sub_f32_e32 v70, v70, v77
	v_sub_f32_e32 v71, v71, v77
	v_sub_f32_e32 v72, v72, v77
	v_cvt_f64_f32_e32 v[84:85], v83
	v_or_b32_e32 v81, 60, v68
	v_or_b32_e32 v82, 61, v69
	v_min_u32_e32 v80, v81, v82
	v_or_b32_e32 v81, 62, v70
	v_or_b32_e32 v82, 63, v71
	v_min3_u32 v80, v80, v81, v82
	v_or_b32_e32 v81, 64, v72
	v_min_u32_e32 v80, v80, v81
	v_mul_f64 v[86:87], v[86:87], v[84:85]
	v_mul_f32_e32 v68, s14, v68
	v_mul_f32_e32 v69, s14, v69
	v_mul_f32_e32 v70, s14, v70
	v_mul_f32_e32 v71, s14, v71
	v_mul_f32_e32 v72, s14, v72
	v_exp_f32_e32 v68, v68
	v_exp_f32_e32 v69, v69
	v_exp_f32_e32 v70, v70
	v_exp_f32_e32 v71, v71
	v_exp_f32_e32 v72, v72
	v_add_f32_e32 v78, v68, v70
	v_add_f32_e32 v79, v69, v71
	v_add_f32_e32 v78, v78, v72
	v_add_f32_e32 v78, v78, v79
	v_cvt_f64_f32_e32 v[84:85], v78
	v_cndmask_b32_e64 v75, v75, v80, s[20:21]
	v_mov_b32_e32 v73, v77
	v_add_f64 v[86:87], v[86:87], v[84:85]
	v_rcp_f64_e32 v[88:89], v[86:87]
	v_cmp_gt_u32_e32 vcc, 64, v75
	s_and_b64 vcc, vcc, s[36:37]
	v_fma_f64 v[90:91], -v[86:87], v[88:89], 1.0
	v_fma_f64 v[88:89], v[90:91], v[88:89], v[88:89]
	v_cvt_f32_f64_e32 v3, v[88:89]
	v_cndmask_b32_e32 v74, 0, v3, vcc
	global_store_dwordx2 v98, v[74:75], s[6:7]
